# GDN step 4: the two 32x32x32 f32 block products (X = L21*T11, T21 = -T22*X) on the matrix cores with v_mfma_f32_16x16x4_f32 (f32 operands, f32 accumulate) instead of VALU FMAs
# baseline (speedup 1.0000x reference)
.Lg4_s1done:
	s_waitcnt lgkmcnt(0)
	s_barrier
	s_lshr_b32 s1, s10, 2
	s_bfe_u32 s11, s10, 0x10001
	s_and_b32 s24, s10, 1
	v_and_b32_e32 v4, 15, v21
	v_lshrrev_b32_e32 v5, 4, v21
	s_mul_i32 s12, s1, 0x3000
	s_mul_i32 s13, s1, 0x4800
	s_add_i32 s12, s12, 0x1b000
	s_mul_i32 s31, s11, 0x1100
	v_mul_u32_u24_e32 v6, 0x110, v4
	s_add_i32 s31, s31, s13
	s_addk_i32 s31, 0x2200
	v_lshl_add_u32 v6, v5, 2, v6
	v_add3_u32 v8, v61, v6, s31
	s_lshl_b32 s31, s24, 6
	v_lshlrev_b32_e32 v7, 7, v5
	s_add_i32 s31, s31, s12
	v_lshl_add_u32 v7, v4, 2, v7
	v_add3_u32 v9, v61, v7, s31
	s_lshl_b32 s35, s11, 11
	v_lshlrev_b32_e32 v10, 7, v4
	s_add_i32 s35, s35, s12
	v_lshl_add_u32 v10, v5, 2, v10
	v_add3_u32 v10, v61, v10, s35
	v_lshlrev_b32_e32 v11, 9, v5
	v_lshl_add_u32 v11, v4, 2, v11
	v_add3_u32 v11, v61, v11, s35
	v_add_u32_e32 v11, s31, v11
	v_subrev_u32_e32 v11, s12, v11
	ds_read_b32 v136, v8 offset:0
	ds_read_b32 v137, v8 offset:16
	ds_read_b32 v138, v8 offset:32
	ds_read_b32 v139, v8 offset:48
	ds_read_b32 v140, v8 offset:64
	ds_read_b32 v141, v8 offset:80
	ds_read_b32 v142, v8 offset:96
	ds_read_b32 v143, v8 offset:112
	ds_read_b32 v144, v9 offset:0
	ds_read_b32 v145, v9 offset:512
	ds_read_b32 v146, v9 offset:1024
	ds_read_b32 v147, v9 offset:1536
	ds_read_b32 v148, v9 offset:2048
	ds_read_b32 v149, v9 offset:2560
	ds_read_b32 v150, v9 offset:3072
	s_waitcnt lgkmcnt(6)
	v_mfma_f32_16x16x4_f32 v[152:155], v136, v144, 0
	ds_read_b32 v151, v9 offset:3584
	s_waitcnt lgkmcnt(6)
	v_mfma_f32_16x16x4_f32 v[152:155], v137, v145, v[152:155]
	s_waitcnt lgkmcnt(5)
	v_mfma_f32_16x16x4_f32 v[152:155], v138, v146, v[152:155]
	s_waitcnt lgkmcnt(4)
	v_mfma_f32_16x16x4_f32 v[152:155], v139, v147, v[152:155]
	s_waitcnt lgkmcnt(3)
	v_mfma_f32_16x16x4_f32 v[152:155], v140, v148, v[152:155]
	s_waitcnt lgkmcnt(2)
	v_mfma_f32_16x16x4_f32 v[152:155], v141, v149, v[152:155]
	s_waitcnt lgkmcnt(1)
	v_mfma_f32_16x16x4_f32 v[152:155], v142, v150, v[152:155]
	s_waitcnt lgkmcnt(0)
	v_mfma_f32_16x16x4_f32 v[152:155], v143, v151, v[152:155]
	s_nop 15
	s_nop 3
	ds_write_b32 v11, v152 offset:8192
	ds_write_b32 v11, v153 offset:8320
	ds_write_b32 v11, v154 offset:8448
	ds_write_b32 v11, v155 offset:8576
	s_waitcnt lgkmcnt(0)
	s_barrier
	s_lshl_b32 s35, s1, 8
	s_lshl_b32 s31, s24, 6
	s_add_i32 s35, s35, s31
	s_add_i32 s35, s35, 0x23200
	v_lshlrev_b32_e32 v12, 2, v4
	v_add3_u32 v12, v61, v12, s35
	ds_read_b32 v136, v10 offset:4096
	ds_read_b32 v137, v10 offset:4112
	ds_read_b32 v138, v10 offset:4128
	ds_read_b32 v139, v10 offset:4144
	ds_read_b32 v140, v10 offset:4160
	ds_read_b32 v141, v10 offset:4176
	ds_read_b32 v142, v10 offset:4192
	ds_read_b32 v143, v10 offset:4208
	ds_read_b32 v144, v9 offset:8192
	ds_read_b32 v145, v9 offset:8704
	ds_read_b32 v146, v9 offset:9216
	ds_read_b32 v147, v9 offset:9728
	ds_read_b32 v148, v9 offset:10240
	ds_read_b32 v149, v9 offset:10752
	ds_read_b32 v150, v9 offset:11264
	s_waitcnt lgkmcnt(6)
	v_mfma_f32_16x16x4_f32 v[152:155], v136, v144, 0
	ds_read_b32 v151, v9 offset:11776
	s_waitcnt lgkmcnt(6)
	v_mfma_f32_16x16x4_f32 v[152:155], v137, v145, v[152:155]
	s_waitcnt lgkmcnt(5)
	v_mfma_f32_16x16x4_f32 v[152:155], v138, v146, v[152:155]
	s_waitcnt lgkmcnt(4)
	v_mfma_f32_16x16x4_f32 v[152:155], v139, v147, v[152:155]
	s_waitcnt lgkmcnt(3)
	v_mfma_f32_16x16x4_f32 v[152:155], v140, v148, v[152:155]
	s_waitcnt lgkmcnt(2)
	v_mfma_f32_16x16x4_f32 v[152:155], v141, v149, v[152:155]
	s_waitcnt lgkmcnt(1)
	v_mfma_f32_16x16x4_f32 v[152:155], v142, v150, v[152:155]
	s_waitcnt lgkmcnt(0)
	v_mfma_f32_16x16x4_f32 v[152:155], v143, v151, v[152:155]
	ds_read_b32 v13, v12
	ds_read_b32 v14, v12 offset:512
	s_mul_i32 s35, s11, 0x900
	v_mul_u32_u24_e32 v15, 0x240, v5
	s_add_i32 s35, s35, s13
	s_addk_i32 s35, 0x1200
	s_lshl_b32 s31, s24, 5
	v_lshl_add_u32 v15, v4, 1, v15
	s_add_i32 s35, s35, s31
	v_add3_u32 v15, v61, v15, s35
	s_waitcnt lgkmcnt(0)
	v_mul_f32_e32 v13, 0x3fb8aa3b, v13
	v_exp_f32_e32 v13, v13
	s_nop 7
	v_mul_f32_e32 v13, v14, v13
	v_mul_f32_e64 v16, -v152, v13
	v_mul_f32_e64 v17, -v152, v14
	v_cvt_pk_bf16_f32 v16, v16, v16
	v_cvt_pk_bf16_f32 v17, v17, v17
	ds_write_b16 v15, v16 offset:0
	ds_write_b16 v15, v17 offset:9216
	v_mul_f32_e64 v16, -v153, v13
	v_mul_f32_e64 v17, -v153, v14
	v_cvt_pk_bf16_f32 v16, v16, v16
	v_cvt_pk_bf16_f32 v17, v17, v17
	ds_write_b16 v15, v16 offset:144
	ds_write_b16 v15, v17 offset:9360
	v_mul_f32_e64 v16, -v154, v13
	v_mul_f32_e64 v17, -v154, v14
	v_cvt_pk_bf16_f32 v16, v16, v16
	v_cvt_pk_bf16_f32 v17, v17, v17
	ds_write_b16 v15, v16 offset:288
	ds_write_b16 v15, v17 offset:9504
	v_mul_f32_e64 v16, -v155, v13
	v_mul_f32_e64 v17, -v155, v14
	v_cvt_pk_bf16_f32 v16, v16, v16
	v_cvt_pk_bf16_f32 v17, v17, v17
	ds_write_b16 v15, v16 offset:432
	ds_write_b16 v15, v17 offset:9648
	s_cmp_gt_u32 s10, 1
	s_cbranch_scc1 .Lg4_done
	s_lshl_b32 s24, s10, 8
	v_lshlrev_b32_e32 v5, 2, v21
	s_add_i32 s24, s24, 0x23200
	v_lshrrev_b32_e32 v4, 5, v21
	v_add3_u32 v12, v61, v5, s24
	ds_read_b32 v13, v12
	ds_read_b32 v14, v12 offset:512
	v_mul_u32_u24_e32 v6, 0x1200, v4
	s_mul_i32 s24, s10, 0x4800
	v_lshl_add_u32 v6, v21, 1, v6
	v_add3_u32 v15, v61, v6, s24
	s_waitcnt lgkmcnt(0)
	v_mul_f32_e32 v13, 0x3fb8aa3b, v13
	v_exp_f32_e32 v13, v13
	s_nop 0
	v_mul_f32_e32 v13, v14, v13
	v_mul_f32_e32 v16, v72, v13
	v_mul_f32_e32 v17, v72, v14
	v_cvt_pk_bf16_f32 v16, v16, v16
	v_cvt_pk_bf16_f32 v17, v17, v17
	ds_write_b16 v15, v16 offset:0
	ds_write_b16 v15, v17 offset:9216
	v_mul_f32_e32 v16, v73, v13
	v_mul_f32_e32 v17, v73, v14
	v_cvt_pk_bf16_f32 v16, v16, v16
	v_cvt_pk_bf16_f32 v17, v17, v17
	ds_write_b16 v15, v16 offset:144
	ds_write_b16 v15, v17 offset:9360
	v_mul_f32_e32 v16, v74, v13
	v_mul_f32_e32 v17, v74, v14
	v_cvt_pk_bf16_f32 v16, v16, v16
	v_cvt_pk_bf16_f32 v17, v17, v17
	ds_write_b16 v15, v16 offset:288
	ds_write_b16 v15, v17 offset:9504
	v_mul_f32_e32 v16, v75, v13
	v_mul_f32_e32 v17, v75, v14
	v_cvt_pk_bf16_f32 v16, v16, v16
	v_cvt_pk_bf16_f32 v17, v17, v17
	ds_write_b16 v15, v16 offset:432
	ds_write_b16 v15, v17 offset:9648
	v_mul_f32_e32 v16, v76, v13
	v_mul_f32_e32 v17, v76, v14
	v_cvt_pk_bf16_f32 v16, v16, v16
	v_cvt_pk_bf16_f32 v17, v17, v17
	ds_write_b16 v15, v16 offset:576
	ds_write_b16 v15, v17 offset:9792
	v_mul_f32_e32 v16, v77, v13
	v_mul_f32_e32 v17, v77, v14
	v_cvt_pk_bf16_f32 v16, v16, v16
	v_cvt_pk_bf16_f32 v17, v17, v17
	ds_write_b16 v15, v16 offset:720
	ds_write_b16 v15, v17 offset:9936
	v_mul_f32_e32 v16, v78, v13
	v_mul_f32_e32 v17, v78, v14
	v_cvt_pk_bf16_f32 v16, v16, v16
	v_cvt_pk_bf16_f32 v17, v17, v17
	ds_write_b16 v15, v16 offset:864
	ds_write_b16 v15, v17 offset:10080
	v_mul_f32_e32 v16, v79, v13
	v_mul_f32_e32 v17, v79, v14
	v_cvt_pk_bf16_f32 v16, v16, v16
	v_cvt_pk_bf16_f32 v17, v17, v17
	ds_write_b16 v15, v16 offset:1008
	ds_write_b16 v15, v17 offset:10224
	v_mul_f32_e32 v16, v80, v13
	v_mul_f32_e32 v17, v80, v14
	v_cvt_pk_bf16_f32 v16, v16, v16
	v_cvt_pk_bf16_f32 v17, v17, v17
	ds_write_b16 v15, v16 offset:1152
	ds_write_b16 v15, v17 offset:10368
	v_mul_f32_e32 v16, v81, v13
	v_mul_f32_e32 v17, v81, v14
	v_cvt_pk_bf16_f32 v16, v16, v16
	v_cvt_pk_bf16_f32 v17, v17, v17
	ds_write_b16 v15, v16 offset:1296
	ds_write_b16 v15, v17 offset:10512
	v_mul_f32_e32 v16, v82, v13
	v_mul_f32_e32 v17, v82, v14
	v_cvt_pk_bf16_f32 v16, v16, v16
	v_cvt_pk_bf16_f32 v17, v17, v17
	ds_write_b16 v15, v16 offset:1440
	ds_write_b16 v15, v17 offset:10656
	v_mul_f32_e32 v16, v83, v13
	v_mul_f32_e32 v17, v83, v14
	v_cvt_pk_bf16_f32 v16, v16, v16
	v_cvt_pk_bf16_f32 v17, v17, v17
	ds_write_b16 v15, v16 offset:1584
	ds_write_b16 v15, v17 offset:10800
	v_mul_f32_e32 v16, v84, v13
	v_mul_f32_e32 v17, v84, v14
	v_cvt_pk_bf16_f32 v16, v16, v16
	v_cvt_pk_bf16_f32 v17, v17, v17
	ds_write_b16 v15, v16 offset:1728
	ds_write_b16 v15, v17 offset:10944
	v_mul_f32_e32 v16, v85, v13
	v_mul_f32_e32 v17, v85, v14
	v_cvt_pk_bf16_f32 v16, v16, v16
	v_cvt_pk_bf16_f32 v17, v17, v17
	ds_write_b16 v15, v16 offset:1872
	ds_write_b16 v15, v17 offset:11088
	v_mul_f32_e32 v16, v86, v13
	v_mul_f32_e32 v17, v86, v14
	v_cvt_pk_bf16_f32 v16, v16, v16
	v_cvt_pk_bf16_f32 v17, v17, v17
	ds_write_b16 v15, v16 offset:2016
	ds_write_b16 v15, v17 offset:11232
	v_mul_f32_e32 v16, v87, v13
	v_mul_f32_e32 v17, v87, v14
	v_cvt_pk_bf16_f32 v16, v16, v16
	v_cvt_pk_bf16_f32 v17, v17, v17
	ds_write_b16 v15, v16 offset:2160
	ds_write_b16 v15, v17 offset:11376
	v_mul_f32_e32 v16, v88, v13
	v_mul_f32_e32 v17, v88, v14
	v_cvt_pk_bf16_f32 v16, v16, v16
	v_cvt_pk_bf16_f32 v17, v17, v17
	ds_write_b16 v15, v16 offset:2304
	ds_write_b16 v15, v17 offset:11520
	v_mul_f32_e32 v16, v89, v13
	v_mul_f32_e32 v17, v89, v14
	v_cvt_pk_bf16_f32 v16, v16, v16
	v_cvt_pk_bf16_f32 v17, v17, v17
	ds_write_b16 v15, v16 offset:2448
	ds_write_b16 v15, v17 offset:11664
	v_mul_f32_e32 v16, v90, v13
	v_mul_f32_e32 v17, v90, v14
	v_cvt_pk_bf16_f32 v16, v16, v16
	v_cvt_pk_bf16_f32 v17, v17, v17
	ds_write_b16 v15, v16 offset:2592
	ds_write_b16 v15, v17 offset:11808
	v_mul_f32_e32 v16, v91, v13
	v_mul_f32_e32 v17, v91, v14
	v_cvt_pk_bf16_f32 v16, v16, v16
	v_cvt_pk_bf16_f32 v17, v17, v17
	ds_write_b16 v15, v16 offset:2736
	ds_write_b16 v15, v17 offset:11952
	v_mul_f32_e32 v16, v92, v13
	v_mul_f32_e32 v17, v92, v14
	v_cvt_pk_bf16_f32 v16, v16, v16
	v_cvt_pk_bf16_f32 v17, v17, v17
	ds_write_b16 v15, v16 offset:2880
	ds_write_b16 v15, v17 offset:12096
	v_mul_f32_e32 v16, v93, v13
	v_mul_f32_e32 v17, v93, v14
	v_cvt_pk_bf16_f32 v16, v16, v16
	v_cvt_pk_bf16_f32 v17, v17, v17
	ds_write_b16 v15, v16 offset:3024
	ds_write_b16 v15, v17 offset:12240
	v_mul_f32_e32 v16, v94, v13
	v_mul_f32_e32 v17, v94, v14
	v_cvt_pk_bf16_f32 v16, v16, v16
	v_cvt_pk_bf16_f32 v17, v17, v17
	ds_write_b16 v15, v16 offset:3168
	ds_write_b16 v15, v17 offset:12384
	v_mul_f32_e32 v16, v95, v13
	v_mul_f32_e32 v17, v95, v14
	v_cvt_pk_bf16_f32 v16, v16, v16
	v_cvt_pk_bf16_f32 v17, v17, v17
	ds_write_b16 v15, v16 offset:3312
	ds_write_b16 v15, v17 offset:12528
	v_mul_f32_e32 v16, v96, v13
	v_mul_f32_e32 v17, v96, v14
	v_cvt_pk_bf16_f32 v16, v16, v16
	v_cvt_pk_bf16_f32 v17, v17, v17
	ds_write_b16 v15, v16 offset:3456
	ds_write_b16 v15, v17 offset:12672
	v_mul_f32_e32 v16, v97, v13
	v_mul_f32_e32 v17, v97, v14
	v_cvt_pk_bf16_f32 v16, v16, v16
	v_cvt_pk_bf16_f32 v17, v17, v17
	ds_write_b16 v15, v16 offset:3600
	ds_write_b16 v15, v17 offset:12816
	v_mul_f32_e32 v16, v98, v13
	v_mul_f32_e32 v17, v98, v14
	v_cvt_pk_bf16_f32 v16, v16, v16
	v_cvt_pk_bf16_f32 v17, v17, v17
	ds_write_b16 v15, v16 offset:3744
	ds_write_b16 v15, v17 offset:12960
	v_mul_f32_e32 v16, v99, v13
	v_mul_f32_e32 v17, v99, v14
	v_cvt_pk_bf16_f32 v16, v16, v16
	v_cvt_pk_bf16_f32 v17, v17, v17
	ds_write_b16 v15, v16 offset:3888
	ds_write_b16 v15, v17 offset:13104
	v_mul_f32_e32 v16, v100, v13
	v_mul_f32_e32 v17, v100, v14
	v_cvt_pk_bf16_f32 v16, v16, v16
	v_cvt_pk_bf16_f32 v17, v17, v17
	ds_write_b16 v15, v16 offset:4032
	ds_write_b16 v15, v17 offset:13248
	v_mul_f32_e32 v16, v101, v13
	v_mul_f32_e32 v17, v101, v14
	v_cvt_pk_bf16_f32 v16, v16, v16
	v_cvt_pk_bf16_f32 v17, v17, v17
	ds_write_b16 v15, v16 offset:4176
	ds_write_b16 v15, v17 offset:13392
	v_mul_f32_e32 v16, v102, v13
	v_mul_f32_e32 v17, v102, v14
	v_cvt_pk_bf16_f32 v16, v16, v16
	v_cvt_pk_bf16_f32 v17, v17, v17
	ds_write_b16 v15, v16 offset:4320
	ds_write_b16 v15, v17 offset:13536
	v_mul_f32_e32 v16, v103, v13
	v_mul_f32_e32 v17, v103, v14
	v_cvt_pk_bf16_f32 v16, v16, v16
	v_cvt_pk_bf16_f32 v17, v17, v17
	ds_write_b16 v15, v16 offset:4464
	ds_write_b16 v15, v17 offset:13680
	v_cmp_lt_u32_e32 vcc, 31, v21
	v_subrev_u32_e32 v18, 0x1200, v15
	v_mov_b32_e32 v19, 0
	s_and_saveexec_b64 s[12:13], vcc
	ds_write_b16 v18, v19 offset:0
	ds_write_b16 v18, v19 offset:9216
	ds_write_b16 v18, v19 offset:144
	ds_write_b16 v18, v19 offset:9360
	ds_write_b16 v18, v19 offset:288
	ds_write_b16 v18, v19 offset:9504
	ds_write_b16 v18, v19 offset:432
	ds_write_b16 v18, v19 offset:9648
	ds_write_b16 v18, v19 offset:576
	ds_write_b16 v18, v19 offset:9792
	ds_write_b16 v18, v19 offset:720
	ds_write_b16 v18, v19 offset:9936
	ds_write_b16 v18, v19 offset:864
	ds_write_b16 v18, v19 offset:10080
	ds_write_b16 v18, v19 offset:1008
	ds_write_b16 v18, v19 offset:10224
	ds_write_b16 v18, v19 offset:1152
	ds_write_b16 v18, v19 offset:10368
	ds_write_b16 v18, v19 offset:1296
	ds_write_b16 v18, v19 offset:10512
	ds_write_b16 v18, v19 offset:1440
	ds_write_b16 v18, v19 offset:10656
	ds_write_b16 v18, v19 offset:1584
	ds_write_b16 v18, v19 offset:10800
	ds_write_b16 v18, v19 offset:1728
	ds_write_b16 v18, v19 offset:10944
	ds_write_b16 v18, v19 offset:1872
	ds_write_b16 v18, v19 offset:11088
	ds_write_b16 v18, v19 offset:2016
	ds_write_b16 v18, v19 offset:11232
	ds_write_b16 v18, v19 offset:2160
	ds_write_b16 v18, v19 offset:11376
	ds_write_b16 v18, v19 offset:2304
	ds_write_b16 v18, v19 offset:11520
	ds_write_b16 v18, v19 offset:2448
	ds_write_b16 v18, v19 offset:11664
	ds_write_b16 v18, v19 offset:2592
	ds_write_b16 v18, v19 offset:11808
	ds_write_b16 v18, v19 offset:2736
	ds_write_b16 v18, v19 offset:11952
	ds_write_b16 v18, v19 offset:2880
	ds_write_b16 v18, v19 offset:12096
	ds_write_b16 v18, v19 offset:3024
	ds_write_b16 v18, v19 offset:12240
	ds_write_b16 v18, v19 offset:3168
	ds_write_b16 v18, v19 offset:12384
	ds_write_b16 v18, v19 offset:3312
	ds_write_b16 v18, v19 offset:12528
	ds_write_b16 v18, v19 offset:3456
	ds_write_b16 v18, v19 offset:12672
	ds_write_b16 v18, v19 offset:3600
	ds_write_b16 v18, v19 offset:12816
	ds_write_b16 v18, v19 offset:3744
	ds_write_b16 v18, v19 offset:12960
	ds_write_b16 v18, v19 offset:3888
	ds_write_b16 v18, v19 offset:13104
	ds_write_b16 v18, v19 offset:4032
	ds_write_b16 v18, v19 offset:13248
	ds_write_b16 v18, v19 offset:4176
	ds_write_b16 v18, v19 offset:13392
	ds_write_b16 v18, v19 offset:4320
	ds_write_b16 v18, v19 offset:13536
	ds_write_b16 v18, v19 offset:4464
	ds_write_b16 v18, v19 offset:13680
	s_or_b64 exec, exec, s[12:13]
